# v60 + MoBA gathered-list entry of the next task loaded one task ahead (15 K buffers)
# speedup vs baseline: 1.0039x; 1.0039x over previous
; template <int DQK, int KB>
; __device__ __forceinline__ void qkt(f32x16& p0, f32x16& p1, const char* K_lds, int r32, int hi, const bf16x8* qr) {
;     constexpr int ROWB = DQK * 2, SHM_K = 64 * ROWB;
;     p0 = f32x16{}; p1 = f32x16{};
;     const char* kb[4];
; #pragma unroll
;     for (int dd = 0; dd < 4; ++dd) kb[dd] = K_lds + KB * SHM_K + r32 * ROWB + (((dd * 16 + hi * 8) * 2) ^ ((r32 & 7) << 4));
; #pragma unroll
;     for (int d0 = 0; d0 < DQK / 16; ++d0) { const char* a = kb[d0 & 3] + (d0 >> 2) * 128;
;         bf16x8 b0 = *reinterpret_cast<const bf16x8*>(a);
;         bf16x8 b1 = *reinterpret_cast<const bf16x8*>(a + 32 * ROWB);
;         p0 = __builtin_amdgcn_mfma_f32_32x32x16_bf16(b0, qr[d0], p0, 0, 0, 0);
;         p1 = __builtin_amdgcn_mfma_f32_32x32x16_bf16(b1, qr[d0], p1, 0, 0, 0); }
.LBB0_548:
	s_or_b64 exec, exec, s[8:9]
	v_readlane_b32 s8, v255, 19
	v_readlane_b32 s10, v255, 21
	v_readlane_b32 s11, v255, 22
	v_add_u32_e32 v2, 0xffffff80, v165
	v_mov_b32_e32 v3, 0
	v_cmp_gt_u32_e32 vcc, s8, v2
	s_and_saveexec_b64 s[8:9], vcc
	v_lshl_add_u64 v[2:3], v[2:3], 2, s[10:11]
	global_load_dword v250, v[2:3], off
	s_or_b64 exec, exec, s[8:9]
	v_readlane_b32 s8, v255, 18
	v_subrev_u32_e32 v132, s77, v134
	s_nop 0
	v_add_u32_e32 v2, s8, v134
	s_movk_i32 s8, 0x2200
	v_mad_i64_i32 v[2:3], s[8:9], v2, s8, v[140:141]
	global_load_dwordx4 v[126:129], v[2:3], off
	global_load_dwordx4 v[122:125], v[2:3], off offset:32
	global_load_dwordx4 v[118:121], v[2:3], off offset:64
	global_load_dwordx4 v[114:117], v[2:3], off offset:96
	global_load_dwordx4 v[110:113], v[2:3], off offset:128
	global_load_dwordx4 v[106:109], v[2:3], off offset:160
	global_load_dwordx4 v[102:105], v[2:3], off offset:192
	global_load_dwordx4 v[98:101], v[2:3], off offset:224
	s_cmp_gt_u32 s80, 1
	ds_read_b128 v[190:193], v166
	ds_read_b128 v[194:197], v166 offset:8192
	ds_read_b128 v[198:201], v167
	ds_read_b128 v[202:205], v167 offset:8192
	ds_read_b128 v[206:209], v168
	ds_read_b128 v[210:213], v168 offset:8192
	ds_read_b128 v[214:217], v169
	ds_read_b128 v[218:221], v169 offset:8192
	ds_read_b128 v[222:225], v166 offset:128
	ds_read_b128 v[226:229], v166 offset:8320
	ds_read_b128 v[230:233], v167 offset:128
	ds_read_b128 v[234:237], v167 offset:8320
	ds_read_b128 v[238:241], v168 offset:128
	s_waitcnt vmcnt(7) lgkmcnt(12)
	v_mfma_f32_32x32x16_bf16 v[18:33], v[190:193], v[126:129], 0
	ds_read_b128 v[242:245], v168 offset:8320
	s_waitcnt lgkmcnt(12)
	v_mfma_f32_32x32x16_bf16 v[2:17], v[194:197], v[126:129], 0
	ds_read_b128 v[246:249], v169 offset:128
	s_waitcnt vmcnt(6) lgkmcnt(12)
	v_mfma_f32_32x32x16_bf16 v[18:33], v[198:201], v[122:125], v[18:33]
	ds_read_b128 v[198:201], v169 offset:8320
	s_waitcnt lgkmcnt(12)
	v_mfma_f32_32x32x16_bf16 v[2:17], v[202:205], v[122:125], v[2:17]
	s_waitcnt vmcnt(5) lgkmcnt(11)
	v_mfma_f32_32x32x16_bf16 v[18:33], v[206:209], v[118:121], v[18:33]
	s_waitcnt lgkmcnt(10)
	v_mfma_f32_32x32x16_bf16 v[2:17], v[210:213], v[118:121], v[2:17]
	s_waitcnt vmcnt(4) lgkmcnt(9)
	v_mfma_f32_32x32x16_bf16 v[18:33], v[214:217], v[114:117], v[18:33]
	s_waitcnt lgkmcnt(8)
	v_mfma_f32_32x32x16_bf16 v[2:17], v[218:221], v[114:117], v[2:17]
	s_waitcnt vmcnt(3) lgkmcnt(7)
	v_mfma_f32_32x32x16_bf16 v[18:33], v[222:225], v[110:113], v[18:33]
	s_waitcnt lgkmcnt(6)
	v_mfma_f32_32x32x16_bf16 v[2:17], v[226:229], v[110:113], v[2:17]
	s_waitcnt vmcnt(2) lgkmcnt(5)
	v_mfma_f32_32x32x16_bf16 v[18:33], v[230:233], v[106:109], v[18:33]
	s_waitcnt lgkmcnt(4)
	v_mfma_f32_32x32x16_bf16 v[2:17], v[234:237], v[106:109], v[2:17]
	s_waitcnt vmcnt(1) lgkmcnt(3)
	v_mfma_f32_32x32x16_bf16 v[18:33], v[238:241], v[102:105], v[18:33]
	s_waitcnt lgkmcnt(2)
	v_mfma_f32_32x32x16_bf16 v[2:17], v[242:245], v[102:105], v[2:17]
	s_waitcnt vmcnt(0) lgkmcnt(1)
	v_mfma_f32_32x32x16_bf16 v[18:33], v[246:249], v[98:101], v[18:33]
	v_mov_b32_e32 v34, v151
	s_nop 0
	v_mul_f32_e32 v36, v34, v155
	v_fma_f32 v42, v34, s34, v36
	v_fma_f32 v43, v34, s35, v36
	v_fma_f32 v44, v34, s2, v36
	v_fma_f32 v45, v34, s3, v36
	v_pk_fma_f32 v[46:47], v[34:35], s[36:37], v[36:37] op_sel_hi:[0,1,0]
	s_waitcnt lgkmcnt(0)
	s_waitcnt lgkmcnt(0)
	v_mfma_f32_32x32x16_bf16 v[2:17], v[198:201], v[98:101], v[2:17]
	v_mov_b32_e32 v41, v34
	v_mul_f32_e32 v38, 0x42000000, v34
	v_fma_f32 v40, 0, v34, v36
	v_fmac_f32_e32 v41, v41, v155
	v_fma_f32 v48, v34, s38, v36
	v_fma_f32 v49, v34, s39, v36
	v_pk_fma_f32 v[50:51], v[34:35], s[40:41], v[36:37] op_sel_hi:[0,1,0]
	v_pk_fma_f32 v[52:53], v[34:35], s[42:43], v[36:37] op_sel_hi:[0,1,0]
	v_pk_fma_f32 v[34:35], v[34:35], s[44:45], v[36:37] op_sel_hi:[0,1,0]
	v_pk_add_f32 v[32:33], v[32:33], v[34:35]
	v_pk_add_f32 v[28:29], v[28:29], v[50:51]
	v_pk_add_f32 v[26:27], v[26:27], v[48:49]
	v_pk_add_f32 v[24:25], v[24:25], v[46:47]
	v_pk_add_f32 v[22:23], v[22:23], v[44:45]
	v_pk_add_f32 v[20:21], v[20:21], v[42:43]
	v_pk_add_f32 v[54:55], v[38:39], v[42:43] op_sel_hi:[0,1]
	v_pk_add_f32 v[44:45], v[38:39], v[44:45] op_sel_hi:[0,1]
	v_pk_add_f32 v[42:43], v[38:39], v[46:47] op_sel_hi:[0,1]
	v_pk_add_f32 v[46:47], v[38:39], v[48:49] op_sel_hi:[0,1]
	v_pk_add_f32 v[48:49], v[38:39], v[50:51] op_sel_hi:[0,1]
	v_pk_add_f32 v[36:37], v[38:39], v[52:53] op_sel_hi:[0,1]
	v_pk_add_f32 v[34:35], v[38:39], v[34:35] op_sel_hi:[0,1]
	v_pk_add_f32 v[50:51], v[38:39], v[40:41] op_sel_hi:[0,1]
	v_pk_add_f32 v[30:31], v[30:31], v[52:53]
	v_pk_add_f32 v[18:19], v[18:19], v[40:41]
	v_pk_add_f32 v[34:35], v[16:17], v[34:35]
	v_pk_add_f32 v[36:37], v[14:15], v[36:37]
	v_pk_add_f32 v[38:39], v[12:13], v[48:49]
	v_pk_add_f32 v[40:41], v[10:11], v[46:47]
	v_pk_add_f32 v[42:43], v[8:9], v[42:43]
	v_pk_add_f32 v[44:45], v[6:7], v[44:45]
	v_pk_add_f32 v[46:47], v[4:5], v[54:55]
	v_pk_add_f32 v[48:49], v[2:3], v[50:51]
	s_cbranch_scc1 .LBB0_550
; __device__ __forceinline__ void mask_tile(f32x16& p0, f32x16& p1, int dq) {
;     const float NEG = -__builtin_inff();
; #pragma unroll
;     for (int r = 0; r < 16; ++r) {
;         const int c = (r & 3) + 8 * (r >> 2);
;         if (dq - c < 0) p0[r] = NEG;
;         if (dq - c - 32 < 0) p1[r] = NEG;
;     }
; }
	v_sub_u32_e32 v2, v132, v154
	v_cmp_gt_i32_e64 s[66:67], 26, v2
	v_cmp_gt_i32_e64 s[68:69], 27, v2
	v_cmp_gt_i32_e64 s[64:65], 25, v2
	s_and_b64 s[66:67], s[68:69], s[66:67]
	v_cmp_gt_i32_e64 s[62:63], 24, v2
	s_and_b64 s[64:65], s[66:67], s[64:65]
	v_cmp_gt_i32_e64 s[60:61], 19, v2
	s_and_b64 s[62:63], s[64:65], s[62:63]
	v_cmp_gt_i32_e64 s[58:59], 18, v2
	s_and_b64 s[60:61], s[62:63], s[60:61]
	v_cmp_gt_i32_e64 s[56:57], 17, v2
	s_and_b64 s[58:59], s[60:61], s[58:59]
	v_cmp_gt_i32_e64 s[54:55], 16, v2
	s_and_b64 s[56:57], s[58:59], s[56:57]
	v_cmp_gt_i32_e64 s[52:53], 11, v2
	s_and_b64 s[54:55], s[56:57], s[54:55]
	v_cmp_gt_i32_e64 s[50:51], 10, v2
	s_and_b64 s[52:53], s[54:55], s[52:53]
	v_cmp_gt_i32_e64 s[48:49], 9, v2
	s_and_b64 s[50:51], s[52:53], s[50:51]
	v_cmp_gt_i32_e64 s[46:47], 8, v2
	s_and_b64 s[48:49], s[50:51], s[48:49]
	v_cmp_gt_i32_e64 s[44:45], 3, v2
	s_and_b64 s[46:47], s[48:49], s[46:47]
	v_cmp_gt_i32_e64 s[42:43], 2, v2
	s_and_b64 s[44:45], s[46:47], s[44:45]
	v_cmp_gt_i32_e64 s[40:41], 1, v2
	s_and_b64 s[42:43], s[44:45], s[42:43]
	v_cmp_gt_i32_e64 s[38:39], 0, v2
	s_and_b64 s[40:41], s[42:43], s[40:41]
	s_and_b64 s[38:39], s[40:41], s[38:39]
	v_cmp_gt_i32_e64 s[36:37], 58, v2
	v_cndmask_b32_e64 v18, v18, v147, s[38:39]
	v_cmp_gt_i32_e64 s[38:39], 59, v2
	v_cmp_gt_i32_e64 s[34:35], 57, v2
	s_and_b64 s[36:37], s[38:39], s[36:37]
	v_cmp_gt_i32_e64 s[30:31], 56, v2
	s_and_b64 s[34:35], s[36:37], s[34:35]
	v_cmp_gt_i32_e64 s[28:29], 51, v2
	s_and_b64 s[30:31], s[34:35], s[30:31]
	v_cmp_gt_i32_e64 s[26:27], 50, v2
	s_and_b64 s[28:29], s[30:31], s[28:29]
	v_cmp_gt_i32_e64 s[24:25], 49, v2
	s_and_b64 s[26:27], s[28:29], s[26:27]
	v_cmp_gt_i32_e64 s[22:23], 48, v2
	s_and_b64 s[24:25], s[26:27], s[24:25]
	v_cmp_gt_i32_e64 s[20:21], 43, v2
	s_and_b64 s[22:23], s[24:25], s[22:23]
	v_cmp_gt_i32_e64 s[18:19], 42, v2
	s_and_b64 s[20:21], s[22:23], s[20:21]
	v_cmp_gt_i32_e64 s[16:17], 41, v2
	s_and_b64 s[18:19], s[20:21], s[18:19]
	v_cmp_gt_i32_e64 s[14:15], 40, v2
	s_and_b64 s[16:17], s[18:19], s[16:17]
	v_cmp_gt_i32_e64 s[12:13], 35, v2
	s_and_b64 s[14:15], s[16:17], s[14:15]
	v_cmp_gt_i32_e64 s[10:11], 34, v2
	s_and_b64 s[12:13], s[14:15], s[12:13]
	v_cmp_gt_i32_e64 s[8:9], 33, v2
	s_and_b64 s[10:11], s[12:13], s[10:11]
	v_cmp_gt_i32_e32 vcc, 32, v2
	s_and_b64 s[8:9], s[10:11], s[8:9]
	v_cndmask_b32_e64 v21, v21, v147, s[44:45]
	s_mov_b32 s44, 0x41d00000
	v_cndmask_b32_e64 v20, v20, v147, s[42:43]
	s_mov_b32 s42, 0x41c00000
	v_cndmask_b32_e64 v19, v19, v147, s[40:41]
	s_mov_b32 s40, 0x41900000
	v_cndmask_b32_e64 v35, v35, v147, s[38:39]
	s_mov_b32 s38, 0x41800000
	v_cndmask_b32_e64 v34, v34, v147, s[36:37]
	s_mov_b32 s36, 0x41200000
	v_cndmask_b32_e64 v37, v37, v147, s[34:35]
	s_mov_b32 s34, 2.0
	s_and_b64 vcc, s[8:9], vcc
	v_cndmask_b32_e64 v33, v33, v147, s[68:69]
	v_cndmask_b32_e64 v32, v32, v147, s[66:67]
	v_cndmask_b32_e64 v31, v31, v147, s[64:65]
	v_cndmask_b32_e64 v30, v30, v147, s[62:63]
	v_cndmask_b32_e64 v29, v29, v147, s[60:61]
	v_cndmask_b32_e64 v28, v28, v147, s[58:59]
	v_cndmask_b32_e64 v27, v27, v147, s[56:57]
	v_cndmask_b32_e64 v26, v26, v147, s[54:55]
	v_cndmask_b32_e64 v25, v25, v147, s[52:53]
	v_cndmask_b32_e64 v24, v24, v147, s[50:51]
	v_cndmask_b32_e64 v23, v23, v147, s[48:49]
	v_cndmask_b32_e64 v22, v22, v147, s[46:47]
	s_mov_b32 s45, 0x41d80000
	s_mov_b32 s43, 0x41c80000
	s_mov_b32 s41, 0x41980000
	s_mov_b32 s39, 0x41880000
	s_mov_b32 s37, 0x41300000
	s_mov_b32 s35, 0x40400000
	v_cndmask_b32_e64 v36, v36, v147, s[30:31]
	v_cndmask_b32_e64 v39, v39, v147, s[28:29]
	v_cndmask_b32_e64 v38, v38, v147, s[26:27]
	v_cndmask_b32_e64 v41, v41, v147, s[24:25]
	v_cndmask_b32_e64 v40, v40, v147, s[22:23]
	v_cndmask_b32_e64 v43, v43, v147, s[20:21]
	v_cndmask_b32_e64 v42, v42, v147, s[18:19]
	v_cndmask_b32_e64 v45, v45, v147, s[16:17]
	v_cndmask_b32_e64 v44, v44, v147, s[14:15]
	v_cndmask_b32_e64 v47, v47, v147, s[12:13]
	v_cndmask_b32_e64 v46, v46, v147, s[10:11]
	v_cndmask_b32_e64 v49, v49, v147, s[8:9]
	v_cndmask_b32_e32 v48, v48, v147, vcc

; __device__ __forceinline__ void p4_moba_loop(Frame& F, const Args& A, const int qo, const bool cvmode) {
;     ...
;             const bool own = tk < 8; int pos, sid;
;             if (own) { pos = n * 256 + tk * 32 + r32; sid = ((b * SEQ + pos) * 8 + h) * 4 + 3; }
;             else { const int idx = (tk - 8) * 32 + r32; pos = 0; sid = PO_DUMP;
;                    if (idx < cnt) { const int ent = WSP(int, WS_LIST)[(size_t)L * 8192 + idx]; pos = ent & 8191; sid = ((b * SEQ + pos) * 8 + h) * 4 + (ent >> 13); } }
.LBB0_554:
	v_add_u32_e32 v132, 0xffffff00, v165
	v_readlane_b32 s8, v255, 19
	v_mov_b32_e32 v144, 0x80000
	v_mov_b32_e32 v134, 0
	v_cmp_gt_i32_e32 vcc, s8, v132
	s_and_saveexec_b64 s[8:9], vcc
	s_cbranch_execz .LBB0_556
	v_readlane_b32 s10, v255, 18
	v_and_b32_e32 v134, 0x1fff, v250
	s_nop 0
	v_or_b32_e32 v3, s10, v134
	v_lshlrev_b32_e32 v3, 5, v3
	v_ashrrev_i32_e32 v2, 13, v250
	v_readlane_b32 s10, v255, 23
	s_nop 1
	v_add3_u32 v144, v2, s10, v3

; template <int DQK, int KB>
; __device__ __forceinline__ void qkt(f32x16& p0, f32x16& p1, const char* K_lds, int r32, int hi, const bf16x8* qr) {
;     constexpr int ROWB = DQK * 2, SHM_K = 64 * ROWB;
;     p0 = f32x16{}; p1 = f32x16{};
;     const char* kb[4];
; #pragma unroll
;     for (int dd = 0; dd < 4; ++dd) kb[dd] = K_lds + KB * SHM_K + r32 * ROWB + (((dd * 16 + hi * 8) * 2) ^ ((r32 & 7) << 4));
; #pragma unroll
;     for (int d0 = 0; d0 < DQK / 16; ++d0) { const char* a = kb[d0 & 3] + (d0 >> 2) * 128;
;         bf16x8 b0 = *reinterpret_cast<const bf16x8*>(a);
;         bf16x8 b1 = *reinterpret_cast<const bf16x8*>(a + 32 * ROWB);
;         p0 = __builtin_amdgcn_mfma_f32_32x32x16_bf16(b0, qr[d0], p0, 0, 0, 0);
;         p1 = __builtin_amdgcn_mfma_f32_32x32x16_bf16(b1, qr[d0], p1, 0, 0, 0); }
.LBB0_692:
	s_cmp_gt_u32 s80, 3
	ds_read_b128 v[190:193], v166 offset:16384
	ds_read_b128 v[194:197], v166 offset:24576
	ds_read_b128 v[198:201], v167 offset:16384
	ds_read_b128 v[202:205], v167 offset:24576
	ds_read_b128 v[206:209], v168 offset:16384
	ds_read_b128 v[210:213], v168 offset:24576
	ds_read_b128 v[214:217], v169 offset:16384
	ds_read_b128 v[218:221], v169 offset:24576
	ds_read_b128 v[222:225], v166 offset:16512
	ds_read_b128 v[226:229], v166 offset:24704
	ds_read_b128 v[230:233], v167 offset:16512
	ds_read_b128 v[234:237], v167 offset:24704
	ds_read_b128 v[238:241], v168 offset:16512
	s_waitcnt lgkmcnt(12)
	v_mfma_f32_32x32x16_bf16 v[82:97], v[190:193], v[126:129], 0
	ds_read_b128 v[242:245], v168 offset:24704
	s_waitcnt lgkmcnt(12)
	v_mfma_f32_32x32x16_bf16 v[66:81], v[194:197], v[126:129], 0
	ds_read_b128 v[246:249], v169 offset:16512
	s_waitcnt lgkmcnt(12)
	v_mfma_f32_32x32x16_bf16 v[82:97], v[198:201], v[122:125], v[82:97]
	ds_read_b128 v[198:201], v169 offset:24704
	s_waitcnt lgkmcnt(12)
	v_mfma_f32_32x32x16_bf16 v[66:81], v[202:205], v[122:125], v[66:81]
	s_waitcnt lgkmcnt(11)
	v_mfma_f32_32x32x16_bf16 v[82:97], v[206:209], v[118:121], v[82:97]
	s_waitcnt lgkmcnt(10)
	v_mfma_f32_32x32x16_bf16 v[66:81], v[210:213], v[118:121], v[66:81]
	s_waitcnt lgkmcnt(9)
	v_mfma_f32_32x32x16_bf16 v[82:97], v[214:217], v[114:117], v[82:97]
	s_waitcnt lgkmcnt(8)
	v_mfma_f32_32x32x16_bf16 v[66:81], v[218:221], v[114:117], v[66:81]
	s_waitcnt lgkmcnt(7)
	v_mfma_f32_32x32x16_bf16 v[82:97], v[222:225], v[110:113], v[82:97]
	s_waitcnt lgkmcnt(6)
	v_mfma_f32_32x32x16_bf16 v[66:81], v[226:229], v[110:113], v[66:81]
	s_waitcnt lgkmcnt(5)
	v_mfma_f32_32x32x16_bf16 v[82:97], v[230:233], v[106:109], v[82:97]
	s_waitcnt lgkmcnt(4)
	v_mfma_f32_32x32x16_bf16 v[66:81], v[234:237], v[106:109], v[66:81]
	s_waitcnt lgkmcnt(3)
	v_mfma_f32_32x32x16_bf16 v[82:97], v[238:241], v[102:105], v[82:97]
	s_waitcnt lgkmcnt(2)
	v_mfma_f32_32x32x16_bf16 v[66:81], v[242:245], v[102:105], v[66:81]
	s_waitcnt lgkmcnt(1)
	v_mfma_f32_32x32x16_bf16 v[82:97], v[246:249], v[98:101], v[82:97]
	v_mov_b32_e32 v174, v151
	s_nop 0
	v_mul_f32_e32 v176, v174, v157
	v_fma_f32 v182, v174, s34, v176
	v_fma_f32 v183, v174, s35, v176
	v_fma_f32 v184, v174, s2, v176
	v_fma_f32 v185, v174, s3, v176
	v_pk_fma_f32 v[186:187], v[174:175], s[36:37], v[176:177] op_sel_hi:[0,1,0]
	s_waitcnt lgkmcnt(0)
	s_waitcnt lgkmcnt(0)
	v_mfma_f32_32x32x16_bf16 v[66:81], v[198:201], v[98:101], v[66:81]
	v_mov_b32_e32 v181, v174
	v_mul_f32_e32 v178, 0x42000000, v174
	v_fma_f32 v180, 0, v174, v176
	v_fmac_f32_e32 v181, v181, v157
	v_fma_f32 v188, v174, s38, v176
	v_fma_f32 v189, v174, s39, v176
	v_pk_fma_f32 v[190:191], v[174:175], s[40:41], v[176:177] op_sel_hi:[0,1,0]
	v_pk_fma_f32 v[192:193], v[174:175], s[42:43], v[176:177] op_sel_hi:[0,1,0]
	v_pk_fma_f32 v[174:175], v[174:175], s[44:45], v[176:177] op_sel_hi:[0,1,0]
	v_pk_add_f32 v[96:97], v[96:97], v[174:175]
	v_pk_add_f32 v[92:93], v[92:93], v[190:191]
	v_pk_add_f32 v[90:91], v[90:91], v[188:189]
	v_pk_add_f32 v[88:89], v[88:89], v[186:187]
	v_pk_add_f32 v[86:87], v[86:87], v[184:185]
	v_pk_add_f32 v[84:85], v[84:85], v[182:183]
	v_pk_add_f32 v[176:177], v[178:179], v[182:183] op_sel_hi:[0,1]
	v_pk_add_f32 v[182:183], v[178:179], v[184:185] op_sel_hi:[0,1]
	v_pk_add_f32 v[184:185], v[178:179], v[186:187] op_sel_hi:[0,1]
	v_pk_add_f32 v[186:187], v[178:179], v[188:189] op_sel_hi:[0,1]
	v_pk_add_f32 v[188:189], v[178:179], v[190:191] op_sel_hi:[0,1]
	v_pk_add_f32 v[190:191], v[178:179], v[192:193] op_sel_hi:[0,1]
	v_pk_add_f32 v[174:175], v[178:179], v[174:175] op_sel_hi:[0,1]
	v_pk_add_f32 v[178:179], v[178:179], v[180:181] op_sel_hi:[0,1]
	v_pk_add_f32 v[94:95], v[94:95], v[192:193]
	v_pk_add_f32 v[82:83], v[82:83], v[180:181]
	v_pk_add_f32 v[80:81], v[80:81], v[174:175]
	v_pk_add_f32 v[78:79], v[78:79], v[190:191]
	v_pk_add_f32 v[76:77], v[76:77], v[188:189]
	v_pk_add_f32 v[74:75], v[74:75], v[186:187]
	v_pk_add_f32 v[72:73], v[72:73], v[184:185]
	v_pk_add_f32 v[70:71], v[70:71], v[182:183]
	v_pk_add_f32 v[68:69], v[68:69], v[176:177]
	v_pk_add_f32 v[66:67], v[66:67], v[178:179]
	s_cbranch_scc1 .LBB0_694
; __device__ __forceinline__ void mask_tile(f32x16& p0, f32x16& p1, int dq) {
;     const float NEG = -__builtin_inff();
; #pragma unroll
;     for (int r = 0; r < 16; ++r) {
;         const int c = (r & 3) + 8 * (r >> 2);
;         if (dq - c < 0) p0[r] = NEG;
;         if (dq - c - 32 < 0) p1[r] = NEG;
;     }
; }
	v_sub_u32_e32 v171, v132, v154
	v_subrev_u32_e32 v171, 64, v171
	v_cmp_gt_i32_e64 s[66:67], 26, v171
	v_cmp_gt_i32_e64 s[68:69], 27, v171
	v_cmp_gt_i32_e64 s[64:65], 25, v171
	s_and_b64 s[66:67], s[68:69], s[66:67]
	v_cmp_gt_i32_e64 s[62:63], 24, v171
	s_and_b64 s[64:65], s[66:67], s[64:65]
	v_cmp_gt_i32_e64 s[60:61], 19, v171
	s_and_b64 s[62:63], s[64:65], s[62:63]
	v_cmp_gt_i32_e64 s[58:59], 18, v171
	s_and_b64 s[60:61], s[62:63], s[60:61]
	v_cmp_gt_i32_e64 s[56:57], 17, v171
	s_and_b64 s[58:59], s[60:61], s[58:59]
	v_cmp_gt_i32_e64 s[54:55], 16, v171
	s_and_b64 s[56:57], s[58:59], s[56:57]
	v_cmp_gt_i32_e64 s[52:53], 11, v171
	s_and_b64 s[54:55], s[56:57], s[54:55]
	v_cmp_gt_i32_e64 s[50:51], 10, v171
	s_and_b64 s[52:53], s[54:55], s[52:53]
	v_cmp_gt_i32_e64 s[48:49], 9, v171
	s_and_b64 s[50:51], s[52:53], s[50:51]
	v_cmp_gt_i32_e64 s[46:47], 8, v171
	s_and_b64 s[48:49], s[50:51], s[48:49]
	v_cmp_gt_i32_e64 s[44:45], 3, v171
	s_and_b64 s[46:47], s[48:49], s[46:47]
	v_cmp_gt_i32_e64 s[42:43], 2, v171
	s_and_b64 s[44:45], s[46:47], s[44:45]
	v_cmp_gt_i32_e64 s[40:41], 1, v171
	s_and_b64 s[42:43], s[44:45], s[42:43]
	v_cmp_gt_i32_e64 s[38:39], 0, v171
	s_and_b64 s[40:41], s[42:43], s[40:41]
	s_and_b64 s[38:39], s[40:41], s[38:39]
	v_cmp_gt_i32_e64 s[36:37], 58, v171
	v_cndmask_b32_e64 v82, v82, v147, s[38:39]
	v_cmp_gt_i32_e64 s[38:39], 59, v171
	v_cmp_gt_i32_e64 s[34:35], 57, v171
	s_and_b64 s[36:37], s[38:39], s[36:37]
	v_cmp_gt_i32_e64 s[30:31], 56, v171
	s_and_b64 s[34:35], s[36:37], s[34:35]
	v_cmp_gt_i32_e64 s[28:29], 51, v171
	s_and_b64 s[30:31], s[34:35], s[30:31]
	v_cmp_gt_i32_e64 s[26:27], 50, v171
	s_and_b64 s[28:29], s[30:31], s[28:29]
	v_cmp_gt_i32_e64 s[24:25], 49, v171
	s_and_b64 s[26:27], s[28:29], s[26:27]
	v_cmp_gt_i32_e64 s[22:23], 48, v171
	s_and_b64 s[24:25], s[26:27], s[24:25]
	v_cmp_gt_i32_e64 s[20:21], 43, v171
	s_and_b64 s[22:23], s[24:25], s[22:23]
	v_cmp_gt_i32_e64 s[18:19], 42, v171
	s_and_b64 s[20:21], s[22:23], s[20:21]
	v_cmp_gt_i32_e64 s[16:17], 41, v171
	s_and_b64 s[18:19], s[20:21], s[18:19]
	v_cmp_gt_i32_e64 s[14:15], 40, v171
	s_and_b64 s[16:17], s[18:19], s[16:17]
	v_cmp_gt_i32_e64 s[12:13], 35, v171
	s_and_b64 s[14:15], s[16:17], s[14:15]
	v_cmp_gt_i32_e64 s[10:11], 34, v171
	s_and_b64 s[12:13], s[14:15], s[12:13]
	v_cmp_gt_i32_e64 s[8:9], 33, v171
	s_and_b64 s[10:11], s[12:13], s[10:11]
	v_cmp_gt_i32_e32 vcc, 32, v171
	s_and_b64 s[8:9], s[10:11], s[8:9]
	v_cndmask_b32_e64 v85, v85, v147, s[44:45]
	s_mov_b32 s44, 0x41d00000
	v_cndmask_b32_e64 v84, v84, v147, s[42:43]
	s_mov_b32 s42, 0x41c00000
	v_cndmask_b32_e64 v83, v83, v147, s[40:41]
	s_mov_b32 s40, 0x41900000
	v_cndmask_b32_e64 v81, v81, v147, s[38:39]
	s_mov_b32 s38, 0x41800000
	v_cndmask_b32_e64 v80, v80, v147, s[36:37]
	s_mov_b32 s36, 0x41200000
	v_cndmask_b32_e64 v79, v79, v147, s[34:35]
	s_mov_b32 s34, 2.0
	s_and_b64 vcc, s[8:9], vcc
	v_cndmask_b32_e64 v97, v97, v147, s[68:69]
	v_cndmask_b32_e64 v96, v96, v147, s[66:67]
	v_cndmask_b32_e64 v95, v95, v147, s[64:65]
	v_cndmask_b32_e64 v94, v94, v147, s[62:63]
	v_cndmask_b32_e64 v93, v93, v147, s[60:61]
	v_cndmask_b32_e64 v92, v92, v147, s[58:59]
	v_cndmask_b32_e64 v91, v91, v147, s[56:57]
	v_cndmask_b32_e64 v90, v90, v147, s[54:55]
	v_cndmask_b32_e64 v89, v89, v147, s[52:53]
	v_cndmask_b32_e64 v88, v88, v147, s[50:51]
	v_cndmask_b32_e64 v87, v87, v147, s[48:49]
	v_cndmask_b32_e64 v86, v86, v147, s[46:47]
	s_mov_b32 s45, 0x41d80000
	s_mov_b32 s43, 0x41c80000
	s_mov_b32 s41, 0x41980000
	s_mov_b32 s39, 0x41880000
	s_mov_b32 s37, 0x41300000
	s_mov_b32 s35, 0x40400000
	v_cndmask_b32_e64 v78, v78, v147, s[30:31]
	v_cndmask_b32_e64 v77, v77, v147, s[28:29]
	v_cndmask_b32_e64 v76, v76, v147, s[26:27]
	v_cndmask_b32_e64 v75, v75, v147, s[24:25]
	v_cndmask_b32_e64 v74, v74, v147, s[22:23]
	v_cndmask_b32_e64 v73, v73, v147, s[20:21]
	v_cndmask_b32_e64 v72, v72, v147, s[18:19]
	v_cndmask_b32_e64 v71, v71, v147, s[16:17]
	v_cndmask_b32_e64 v70, v70, v147, s[14:15]
	v_cndmask_b32_e64 v69, v69, v147, s[12:13]
	v_cndmask_b32_e64 v68, v68, v147, s[10:11]
	v_cndmask_b32_e64 v67, v67, v147, s[8:9]
	v_cndmask_b32_e32 v66, v66, v147, vcc

; template <int DQK, int KB>
; __device__ __forceinline__ void qkt(f32x16& p0, f32x16& p1, const char* K_lds, int r32, int hi, const bf16x8* qr) {
;     constexpr int ROWB = DQK * 2, SHM_K = 64 * ROWB;
;     p0 = f32x16{}; p1 = f32x16{};
;     const char* kb[4];
; #pragma unroll
;     for (int dd = 0; dd < 4; ++dd) kb[dd] = K_lds + KB * SHM_K + r32 * ROWB + (((dd * 16 + hi * 8) * 2) ^ ((r32 & 7) << 4));
; #pragma unroll
;     for (int d0 = 0; d0 < DQK / 16; ++d0) { const char* a = kb[d0 & 3] + (d0 >> 2) * 128;
;         bf16x8 b0 = *reinterpret_cast<const bf16x8*>(a);
;         bf16x8 b1 = *reinterpret_cast<const bf16x8*>(a + 32 * ROWB);
;         p0 = __builtin_amdgcn_mfma_f32_32x32x16_bf16(b0, qr[d0], p0, 0, 0, 0);
;         p1 = __builtin_amdgcn_mfma_f32_32x32x16_bf16(b1, qr[d0], p1, 0, 0, 0); }
.LBB0_699:
	s_cmp_gt_u32 s80, 5
	ds_read_b128 v[190:193], v166 offset:32768
	ds_read_b128 v[194:197], v166 offset:40960
	ds_read_b128 v[198:201], v167 offset:32768
	ds_read_b128 v[202:205], v167 offset:40960
	ds_read_b128 v[206:209], v168 offset:32768
	ds_read_b128 v[210:213], v168 offset:40960
	ds_read_b128 v[214:217], v169 offset:32768
	ds_read_b128 v[218:221], v169 offset:40960
	ds_read_b128 v[222:225], v166 offset:32896
	ds_read_b128 v[226:229], v166 offset:41088
	ds_read_b128 v[230:233], v167 offset:32896
	ds_read_b128 v[234:237], v167 offset:41088
	ds_read_b128 v[238:241], v168 offset:32896
	s_waitcnt lgkmcnt(12)
	v_mfma_f32_32x32x16_bf16 v[82:97], v[190:193], v[126:129], 0
	ds_read_b128 v[242:245], v168 offset:41088
	s_waitcnt lgkmcnt(12)
	v_mfma_f32_32x32x16_bf16 v[66:81], v[194:197], v[126:129], 0
	ds_read_b128 v[246:249], v169 offset:32896
	s_waitcnt lgkmcnt(12)
	v_mfma_f32_32x32x16_bf16 v[82:97], v[198:201], v[122:125], v[82:97]
	ds_read_b128 v[198:201], v169 offset:41088
	s_waitcnt lgkmcnt(12)
	v_mfma_f32_32x32x16_bf16 v[66:81], v[202:205], v[122:125], v[66:81]
	s_waitcnt lgkmcnt(11)
	v_mfma_f32_32x32x16_bf16 v[82:97], v[206:209], v[118:121], v[82:97]
	s_waitcnt lgkmcnt(10)
	v_mfma_f32_32x32x16_bf16 v[66:81], v[210:213], v[118:121], v[66:81]
	s_waitcnt lgkmcnt(9)
	v_mfma_f32_32x32x16_bf16 v[82:97], v[214:217], v[114:117], v[82:97]
	s_waitcnt lgkmcnt(8)
	v_mfma_f32_32x32x16_bf16 v[66:81], v[218:221], v[114:117], v[66:81]
	s_waitcnt lgkmcnt(7)
	v_mfma_f32_32x32x16_bf16 v[82:97], v[222:225], v[110:113], v[82:97]
	s_waitcnt lgkmcnt(6)
	v_mfma_f32_32x32x16_bf16 v[66:81], v[226:229], v[110:113], v[66:81]
	s_waitcnt lgkmcnt(5)
	v_mfma_f32_32x32x16_bf16 v[82:97], v[230:233], v[106:109], v[82:97]
	s_waitcnt lgkmcnt(4)
	v_mfma_f32_32x32x16_bf16 v[66:81], v[234:237], v[106:109], v[66:81]
	s_waitcnt lgkmcnt(3)
	v_mfma_f32_32x32x16_bf16 v[82:97], v[238:241], v[102:105], v[82:97]
	s_waitcnt lgkmcnt(2)
	v_mfma_f32_32x32x16_bf16 v[66:81], v[242:245], v[102:105], v[66:81]
	s_waitcnt lgkmcnt(1)
	v_mfma_f32_32x32x16_bf16 v[82:97], v[246:249], v[98:101], v[82:97]
	v_mov_b32_e32 v174, v151
	s_nop 0
	v_mul_f32_e32 v176, v174, v158
	v_fma_f32 v182, v174, s34, v176
	v_fma_f32 v183, v174, s35, v176
	v_fma_f32 v184, v174, s2, v176
	v_fma_f32 v185, v174, s3, v176
	v_pk_fma_f32 v[186:187], v[174:175], s[36:37], v[176:177] op_sel_hi:[0,1,0]
	s_waitcnt lgkmcnt(0)
	s_waitcnt lgkmcnt(0)
	v_mfma_f32_32x32x16_bf16 v[66:81], v[198:201], v[98:101], v[66:81]
	v_mov_b32_e32 v181, v174
	v_mul_f32_e32 v178, 0x42000000, v174
	v_fma_f32 v180, 0, v174, v176
	v_fmac_f32_e32 v181, v181, v158
	v_fma_f32 v188, v174, s38, v176
	v_fma_f32 v189, v174, s39, v176
	v_pk_fma_f32 v[190:191], v[174:175], s[40:41], v[176:177] op_sel_hi:[0,1,0]
	v_pk_fma_f32 v[192:193], v[174:175], s[42:43], v[176:177] op_sel_hi:[0,1,0]
	v_pk_fma_f32 v[174:175], v[174:175], s[44:45], v[176:177] op_sel_hi:[0,1,0]
	v_pk_add_f32 v[96:97], v[96:97], v[174:175]
	v_pk_add_f32 v[92:93], v[92:93], v[190:191]
	v_pk_add_f32 v[90:91], v[90:91], v[188:189]
	v_pk_add_f32 v[88:89], v[88:89], v[186:187]
	v_pk_add_f32 v[86:87], v[86:87], v[184:185]
	v_pk_add_f32 v[84:85], v[84:85], v[182:183]
	v_pk_add_f32 v[176:177], v[178:179], v[182:183] op_sel_hi:[0,1]
	v_pk_add_f32 v[182:183], v[178:179], v[184:185] op_sel_hi:[0,1]
	v_pk_add_f32 v[184:185], v[178:179], v[186:187] op_sel_hi:[0,1]
	v_pk_add_f32 v[186:187], v[178:179], v[188:189] op_sel_hi:[0,1]
	v_pk_add_f32 v[188:189], v[178:179], v[190:191] op_sel_hi:[0,1]
	v_pk_add_f32 v[190:191], v[178:179], v[192:193] op_sel_hi:[0,1]
	v_pk_add_f32 v[174:175], v[178:179], v[174:175] op_sel_hi:[0,1]
	v_pk_add_f32 v[178:179], v[178:179], v[180:181] op_sel_hi:[0,1]
	v_pk_add_f32 v[94:95], v[94:95], v[192:193]
	v_pk_add_f32 v[82:83], v[82:83], v[180:181]
	v_pk_add_f32 v[80:81], v[80:81], v[174:175]
	v_pk_add_f32 v[78:79], v[78:79], v[190:191]
	v_pk_add_f32 v[76:77], v[76:77], v[188:189]
	v_pk_add_f32 v[74:75], v[74:75], v[186:187]
	v_pk_add_f32 v[72:73], v[72:73], v[184:185]
	v_pk_add_f32 v[70:71], v[70:71], v[182:183]
	v_pk_add_f32 v[68:69], v[68:69], v[176:177]
	v_pk_add_f32 v[66:67], v[66:67], v[178:179]
	s_cbranch_scc1 .LBB0_701
; __device__ __forceinline__ void mask_tile(f32x16& p0, f32x16& p1, int dq) {
;     const float NEG = -__builtin_inff();
; #pragma unroll
;     for (int r = 0; r < 16; ++r) {
;         const int c = (r & 3) + 8 * (r >> 2);
;         if (dq - c < 0) p0[r] = NEG;
;         if (dq - c - 32 < 0) p1[r] = NEG;
;     }
; }
	v_sub_u32_e32 v171, v132, v154
	v_add_u32_e32 v171, 0xffffff80, v171
	v_cmp_gt_i32_e64 s[66:67], 26, v171
	v_cmp_gt_i32_e64 s[68:69], 27, v171
	v_cmp_gt_i32_e64 s[64:65], 25, v171
	s_and_b64 s[66:67], s[68:69], s[66:67]
	v_cmp_gt_i32_e64 s[62:63], 24, v171
	s_and_b64 s[64:65], s[66:67], s[64:65]
	v_cmp_gt_i32_e64 s[60:61], 19, v171
	s_and_b64 s[62:63], s[64:65], s[62:63]
	v_cmp_gt_i32_e64 s[58:59], 18, v171
	s_and_b64 s[60:61], s[62:63], s[60:61]
	v_cmp_gt_i32_e64 s[56:57], 17, v171
	s_and_b64 s[58:59], s[60:61], s[58:59]
	v_cmp_gt_i32_e64 s[54:55], 16, v171
	s_and_b64 s[56:57], s[58:59], s[56:57]
	v_cmp_gt_i32_e64 s[52:53], 11, v171
	s_and_b64 s[54:55], s[56:57], s[54:55]
	v_cmp_gt_i32_e64 s[50:51], 10, v171
	s_and_b64 s[52:53], s[54:55], s[52:53]
	v_cmp_gt_i32_e64 s[48:49], 9, v171
	s_and_b64 s[50:51], s[52:53], s[50:51]
	v_cmp_gt_i32_e64 s[46:47], 8, v171
	s_and_b64 s[48:49], s[50:51], s[48:49]
	v_cmp_gt_i32_e64 s[44:45], 3, v171
	s_and_b64 s[46:47], s[48:49], s[46:47]
	v_cmp_gt_i32_e64 s[42:43], 2, v171
	s_and_b64 s[44:45], s[46:47], s[44:45]
	v_cmp_gt_i32_e64 s[40:41], 1, v171
	s_and_b64 s[42:43], s[44:45], s[42:43]
	v_cmp_gt_i32_e64 s[38:39], 0, v171
	s_and_b64 s[40:41], s[42:43], s[40:41]
	s_and_b64 s[38:39], s[40:41], s[38:39]
	v_cmp_gt_i32_e64 s[36:37], 58, v171
	v_cndmask_b32_e64 v82, v82, v147, s[38:39]
	v_cmp_gt_i32_e64 s[38:39], 59, v171
	v_cmp_gt_i32_e64 s[34:35], 57, v171
	s_and_b64 s[36:37], s[38:39], s[36:37]
	v_cmp_gt_i32_e64 s[30:31], 56, v171
	s_and_b64 s[34:35], s[36:37], s[34:35]
	v_cmp_gt_i32_e64 s[28:29], 51, v171
	s_and_b64 s[30:31], s[34:35], s[30:31]
	v_cmp_gt_i32_e64 s[26:27], 50, v171
	s_and_b64 s[28:29], s[30:31], s[28:29]
	v_cmp_gt_i32_e64 s[24:25], 49, v171
	s_and_b64 s[26:27], s[28:29], s[26:27]
	v_cmp_gt_i32_e64 s[22:23], 48, v171
	s_and_b64 s[24:25], s[26:27], s[24:25]
	v_cmp_gt_i32_e64 s[20:21], 43, v171
	s_and_b64 s[22:23], s[24:25], s[22:23]
	v_cmp_gt_i32_e64 s[18:19], 42, v171
	s_and_b64 s[20:21], s[22:23], s[20:21]
	v_cmp_gt_i32_e64 s[16:17], 41, v171
	s_and_b64 s[18:19], s[20:21], s[18:19]
	v_cmp_gt_i32_e64 s[14:15], 40, v171
	s_and_b64 s[16:17], s[18:19], s[16:17]
	v_cmp_gt_i32_e64 s[12:13], 35, v171
	s_and_b64 s[14:15], s[16:17], s[14:15]
	v_cmp_gt_i32_e64 s[10:11], 34, v171
	s_and_b64 s[12:13], s[14:15], s[12:13]
	v_cmp_gt_i32_e64 s[8:9], 33, v171
	s_and_b64 s[10:11], s[12:13], s[10:11]
	v_cmp_gt_i32_e32 vcc, 32, v171
	s_and_b64 s[8:9], s[10:11], s[8:9]
	v_cndmask_b32_e64 v85, v85, v147, s[44:45]
	s_mov_b32 s44, 0x41d00000
	v_cndmask_b32_e64 v84, v84, v147, s[42:43]
	s_mov_b32 s42, 0x41c00000
	v_cndmask_b32_e64 v83, v83, v147, s[40:41]
	s_mov_b32 s40, 0x41900000
	v_cndmask_b32_e64 v81, v81, v147, s[38:39]
	s_mov_b32 s38, 0x41800000
	v_cndmask_b32_e64 v80, v80, v147, s[36:37]
	s_mov_b32 s36, 0x41200000
	v_cndmask_b32_e64 v79, v79, v147, s[34:35]
	s_mov_b32 s34, 2.0
	s_and_b64 vcc, s[8:9], vcc
	v_cndmask_b32_e64 v97, v97, v147, s[68:69]
	v_cndmask_b32_e64 v96, v96, v147, s[66:67]
	v_cndmask_b32_e64 v95, v95, v147, s[64:65]
	v_cndmask_b32_e64 v94, v94, v147, s[62:63]
	v_cndmask_b32_e64 v93, v93, v147, s[60:61]
	v_cndmask_b32_e64 v92, v92, v147, s[58:59]
	v_cndmask_b32_e64 v91, v91, v147, s[56:57]
	v_cndmask_b32_e64 v90, v90, v147, s[54:55]
	v_cndmask_b32_e64 v89, v89, v147, s[52:53]
	v_cndmask_b32_e64 v88, v88, v147, s[50:51]
	v_cndmask_b32_e64 v87, v87, v147, s[48:49]
	v_cndmask_b32_e64 v86, v86, v147, s[46:47]
	s_mov_b32 s45, 0x41d80000
	s_mov_b32 s43, 0x41c80000
	s_mov_b32 s41, 0x41980000
	s_mov_b32 s39, 0x41880000
	s_mov_b32 s37, 0x41300000
	s_mov_b32 s35, 0x40400000
	v_cndmask_b32_e64 v78, v78, v147, s[30:31]
	v_cndmask_b32_e64 v77, v77, v147, s[28:29]
	v_cndmask_b32_e64 v76, v76, v147, s[26:27]
	v_cndmask_b32_e64 v75, v75, v147, s[24:25]
	v_cndmask_b32_e64 v74, v74, v147, s[22:23]
	v_cndmask_b32_e64 v73, v73, v147, s[20:21]
	v_cndmask_b32_e64 v72, v72, v147, s[18:19]
	v_cndmask_b32_e64 v71, v71, v147, s[16:17]
	v_cndmask_b32_e64 v70, v70, v147, s[14:15]
	v_cndmask_b32_e64 v69, v69, v147, s[12:13]
	v_cndmask_b32_e64 v68, v68, v147, s[10:11]
	v_cndmask_b32_e64 v67, v67, v147, s[8:9]
	v_cndmask_b32_e32 v66, v66, v147, vcc

; template <int DQK, int KB>
; __device__ __forceinline__ void qkt(f32x16& p0, f32x16& p1, const char* K_lds, int r32, int hi, const bf16x8* qr) {
;     constexpr int ROWB = DQK * 2, SHM_K = 64 * ROWB;
;     p0 = f32x16{}; p1 = f32x16{};
;     const char* kb[4];
; #pragma unroll
;     for (int dd = 0; dd < 4; ++dd) kb[dd] = K_lds + KB * SHM_K + r32 * ROWB + (((dd * 16 + hi * 8) * 2) ^ ((r32 & 7) << 4));
; #pragma unroll
;     for (int d0 = 0; d0 < DQK / 16; ++d0) { const char* a = kb[d0 & 3] + (d0 >> 2) * 128;
;         bf16x8 b0 = *reinterpret_cast<const bf16x8*>(a);
;         bf16x8 b1 = *reinterpret_cast<const bf16x8*>(a + 32 * ROWB);
;         p0 = __builtin_amdgcn_mfma_f32_32x32x16_bf16(b0, qr[d0], p0, 0, 0, 0);
;         p1 = __builtin_amdgcn_mfma_f32_32x32x16_bf16(b1, qr[d0], p1, 0, 0, 0); }
.LBB0_706:
	s_andn2_b64 vcc, exec, s[74:75]
	ds_read_b128 v[190:193], v166 offset:49152
	ds_read_b128 v[194:197], v166 offset:57344
	ds_read_b128 v[198:201], v167 offset:49152
	ds_read_b128 v[202:205], v167 offset:57344
	ds_read_b128 v[206:209], v168 offset:49152
	ds_read_b128 v[210:213], v168 offset:57344
	ds_read_b128 v[214:217], v169 offset:49152
	ds_read_b128 v[218:221], v169 offset:57344
	ds_read_b128 v[222:225], v166 offset:49280
	ds_read_b128 v[226:229], v166 offset:57472
	ds_read_b128 v[230:233], v167 offset:49280
	ds_read_b128 v[234:237], v167 offset:57472
	ds_read_b128 v[238:241], v168 offset:49280
	s_waitcnt lgkmcnt(12)
	v_mfma_f32_32x32x16_bf16 v[82:97], v[190:193], v[126:129], 0
	ds_read_b128 v[242:245], v168 offset:57472
	s_waitcnt lgkmcnt(12)
	v_mfma_f32_32x32x16_bf16 v[66:81], v[194:197], v[126:129], 0
	ds_read_b128 v[246:249], v169 offset:49280
	s_waitcnt lgkmcnt(12)
	v_mfma_f32_32x32x16_bf16 v[82:97], v[198:201], v[122:125], v[82:97]
	ds_read_b128 v[198:201], v169 offset:57472
	s_waitcnt lgkmcnt(12)
	v_mfma_f32_32x32x16_bf16 v[66:81], v[202:205], v[122:125], v[66:81]
	s_waitcnt lgkmcnt(11)
	v_mfma_f32_32x32x16_bf16 v[82:97], v[206:209], v[118:121], v[82:97]
	s_waitcnt lgkmcnt(10)
	v_mfma_f32_32x32x16_bf16 v[66:81], v[210:213], v[118:121], v[66:81]
	s_waitcnt lgkmcnt(9)
	v_mfma_f32_32x32x16_bf16 v[82:97], v[214:217], v[114:117], v[82:97]
	s_waitcnt lgkmcnt(8)
	v_mfma_f32_32x32x16_bf16 v[66:81], v[218:221], v[114:117], v[66:81]
	s_waitcnt lgkmcnt(7)
	v_mfma_f32_32x32x16_bf16 v[82:97], v[222:225], v[110:113], v[82:97]
	s_waitcnt lgkmcnt(6)
	v_mfma_f32_32x32x16_bf16 v[66:81], v[226:229], v[110:113], v[66:81]
	s_waitcnt lgkmcnt(5)
	v_mfma_f32_32x32x16_bf16 v[82:97], v[230:233], v[106:109], v[82:97]
	s_waitcnt lgkmcnt(4)
	v_mfma_f32_32x32x16_bf16 v[66:81], v[234:237], v[106:109], v[66:81]
	s_waitcnt lgkmcnt(3)
	v_mfma_f32_32x32x16_bf16 v[82:97], v[238:241], v[102:105], v[82:97]
	s_waitcnt lgkmcnt(2)
	v_mfma_f32_32x32x16_bf16 v[66:81], v[242:245], v[102:105], v[66:81]
	s_waitcnt lgkmcnt(1)
	v_mfma_f32_32x32x16_bf16 v[82:97], v[246:249], v[98:101], v[82:97]
	s_waitcnt lgkmcnt(0)
	v_mfma_f32_32x32x16_bf16 v[66:81], v[198:201], v[98:101], v[66:81]
	v_mov_b32_e32 v98, v151
	s_nop 0
	v_mul_f32_e32 v100, v98, v159
	v_mov_b32_e32 v105, v98
	v_mul_f32_e32 v102, 0x42000000, v98
	v_fma_f32 v104, 0, v98, v100
	v_fmac_f32_e32 v105, v105, v159
	v_pk_fma_f32 v[106:107], v[98:99], s[34:35], v[100:101] op_sel_hi:[0,1,0]
	v_pk_fma_f32 v[108:109], v[98:99], s[2:3], v[100:101] op_sel_hi:[0,1,0]
	v_pk_fma_f32 v[110:111], v[98:99], s[36:37], v[100:101] op_sel_hi:[0,1,0]
	v_pk_fma_f32 v[112:113], v[98:99], s[38:39], v[100:101] op_sel_hi:[0,1,0]
	v_pk_fma_f32 v[114:115], v[98:99], s[40:41], v[100:101] op_sel_hi:[0,1,0]
	v_pk_fma_f32 v[116:117], v[98:99], s[42:43], v[100:101] op_sel_hi:[0,1,0]
	v_pk_fma_f32 v[98:99], v[98:99], s[44:45], v[100:101] op_sel_hi:[0,1,0]
	v_pk_add_f32 v[96:97], v[96:97], v[98:99]
	v_pk_add_f32 v[92:93], v[92:93], v[114:115]
	v_pk_add_f32 v[90:91], v[90:91], v[112:113]
	v_pk_add_f32 v[88:89], v[88:89], v[110:111]
	v_pk_add_f32 v[86:87], v[86:87], v[108:109]
	v_pk_add_f32 v[84:85], v[84:85], v[106:107]
	v_pk_add_f32 v[100:101], v[102:103], v[106:107] op_sel_hi:[0,1]
	v_pk_add_f32 v[106:107], v[102:103], v[108:109] op_sel_hi:[0,1]
	v_pk_add_f32 v[108:109], v[102:103], v[110:111] op_sel_hi:[0,1]
	v_pk_add_f32 v[110:111], v[102:103], v[112:113] op_sel_hi:[0,1]
	v_pk_add_f32 v[112:113], v[102:103], v[114:115] op_sel_hi:[0,1]
	v_pk_add_f32 v[114:115], v[102:103], v[116:117] op_sel_hi:[0,1]
	v_pk_add_f32 v[98:99], v[102:103], v[98:99] op_sel_hi:[0,1]
	v_pk_add_f32 v[102:103], v[102:103], v[104:105] op_sel_hi:[0,1]
	v_pk_add_f32 v[94:95], v[94:95], v[116:117]
	v_pk_add_f32 v[82:83], v[82:83], v[104:105]
	v_pk_add_f32 v[80:81], v[80:81], v[98:99]
	v_pk_add_f32 v[78:79], v[78:79], v[114:115]
	v_pk_add_f32 v[76:77], v[76:77], v[112:113]
	v_pk_add_f32 v[74:75], v[74:75], v[110:111]
	v_pk_add_f32 v[72:73], v[72:73], v[108:109]
	v_pk_add_f32 v[70:71], v[70:71], v[106:107]
	v_pk_add_f32 v[68:69], v[68:69], v[100:101]
	v_pk_add_f32 v[66:67], v[66:67], v[102:103]
	s_cbranch_vccnz .LBB0_708
; __device__ __forceinline__ void mask_tile(f32x16& p0, f32x16& p1, int dq) {
;     const float NEG = -__builtin_inff();
; #pragma unroll
;     for (int r = 0; r < 16; ++r) {
;         const int c = (r & 3) + 8 * (r >> 2);
;         if (dq - c < 0) p0[r] = NEG;
;         if (dq - c - 32 < 0) p1[r] = NEG;
;     }
; }
	v_sub_u32_e32 v98, v132, v154
	v_add_u32_e32 v98, 0xffffff40, v98
	v_cmp_gt_i32_e64 s[66:67], 26, v98
	v_cmp_gt_i32_e64 s[68:69], 27, v98
	v_cmp_gt_i32_e64 s[64:65], 25, v98
	s_and_b64 s[66:67], s[68:69], s[66:67]
	v_cmp_gt_i32_e64 s[62:63], 24, v98
	s_and_b64 s[64:65], s[66:67], s[64:65]
	v_cmp_gt_i32_e64 s[60:61], 19, v98
	s_and_b64 s[62:63], s[64:65], s[62:63]
	v_cmp_gt_i32_e64 s[58:59], 18, v98
	s_and_b64 s[60:61], s[62:63], s[60:61]
	v_cmp_gt_i32_e64 s[56:57], 17, v98
	s_and_b64 s[58:59], s[60:61], s[58:59]
	v_cmp_gt_i32_e64 s[54:55], 16, v98
	s_and_b64 s[56:57], s[58:59], s[56:57]
	v_cmp_gt_i32_e64 s[52:53], 11, v98
	s_and_b64 s[54:55], s[56:57], s[54:55]
	v_cmp_gt_i32_e64 s[50:51], 10, v98
	s_and_b64 s[52:53], s[54:55], s[52:53]
	v_cmp_gt_i32_e64 s[48:49], 9, v98
	s_and_b64 s[50:51], s[52:53], s[50:51]
	v_cmp_gt_i32_e64 s[46:47], 8, v98
	s_and_b64 s[48:49], s[50:51], s[48:49]
	v_cmp_gt_i32_e64 s[44:45], 3, v98
	s_and_b64 s[46:47], s[48:49], s[46:47]
	v_cmp_gt_i32_e64 s[42:43], 2, v98
	s_and_b64 s[44:45], s[46:47], s[44:45]
	v_cmp_gt_i32_e64 s[40:41], 1, v98
	s_and_b64 s[42:43], s[44:45], s[42:43]
	v_cmp_gt_i32_e64 s[38:39], 0, v98
	s_and_b64 s[40:41], s[42:43], s[40:41]
	s_and_b64 s[38:39], s[40:41], s[38:39]
	v_cmp_gt_i32_e64 s[36:37], 58, v98
	v_cndmask_b32_e64 v82, v82, v147, s[38:39]
	v_cmp_gt_i32_e64 s[38:39], 59, v98
	v_cmp_gt_i32_e64 s[34:35], 57, v98
	s_and_b64 s[36:37], s[38:39], s[36:37]
	v_cmp_gt_i32_e64 s[30:31], 56, v98
	s_and_b64 s[34:35], s[36:37], s[34:35]
	v_cmp_gt_i32_e64 s[28:29], 51, v98
	s_and_b64 s[30:31], s[34:35], s[30:31]
	v_cmp_gt_i32_e64 s[26:27], 50, v98
	s_and_b64 s[28:29], s[30:31], s[28:29]
	v_cmp_gt_i32_e64 s[24:25], 49, v98
	s_and_b64 s[26:27], s[28:29], s[26:27]
	v_cmp_gt_i32_e64 s[22:23], 48, v98
	s_and_b64 s[24:25], s[26:27], s[24:25]
	v_cmp_gt_i32_e64 s[20:21], 43, v98
	s_and_b64 s[22:23], s[24:25], s[22:23]
	v_cmp_gt_i32_e64 s[18:19], 42, v98
	s_and_b64 s[20:21], s[22:23], s[20:21]
	v_cmp_gt_i32_e64 s[16:17], 41, v98
	s_and_b64 s[18:19], s[20:21], s[18:19]
	v_cmp_gt_i32_e64 s[14:15], 40, v98
	s_and_b64 s[16:17], s[18:19], s[16:17]
	v_cmp_gt_i32_e64 s[12:13], 35, v98
	s_and_b64 s[14:15], s[16:17], s[14:15]
	v_cmp_gt_i32_e64 s[10:11], 34, v98
	s_and_b64 s[12:13], s[14:15], s[12:13]
	v_cmp_gt_i32_e64 s[8:9], 33, v98
	s_and_b64 s[10:11], s[12:13], s[10:11]
	v_cmp_gt_i32_e32 vcc, 32, v98
	s_and_b64 s[8:9], s[10:11], s[8:9]
	v_cndmask_b32_e64 v85, v85, v147, s[44:45]
	s_mov_b32 s44, 0x41d00000
	v_cndmask_b32_e64 v84, v84, v147, s[42:43]
	s_mov_b32 s42, 0x41c00000
	v_cndmask_b32_e64 v83, v83, v147, s[40:41]
	s_mov_b32 s40, 0x41900000
	v_cndmask_b32_e64 v81, v81, v147, s[38:39]
	s_mov_b32 s38, 0x41800000
	v_cndmask_b32_e64 v80, v80, v147, s[36:37]
	s_mov_b32 s36, 0x41200000
	v_cndmask_b32_e64 v79, v79, v147, s[34:35]
	s_mov_b32 s34, 2.0
	s_and_b64 vcc, s[8:9], vcc
	v_cndmask_b32_e64 v97, v97, v147, s[68:69]
	v_cndmask_b32_e64 v96, v96, v147, s[66:67]
	v_cndmask_b32_e64 v95, v95, v147, s[64:65]
	v_cndmask_b32_e64 v94, v94, v147, s[62:63]
	v_cndmask_b32_e64 v93, v93, v147, s[60:61]
	v_cndmask_b32_e64 v92, v92, v147, s[58:59]
	v_cndmask_b32_e64 v91, v91, v147, s[56:57]
	v_cndmask_b32_e64 v90, v90, v147, s[54:55]
	v_cndmask_b32_e64 v89, v89, v147, s[52:53]
	v_cndmask_b32_e64 v88, v88, v147, s[50:51]
	v_cndmask_b32_e64 v87, v87, v147, s[48:49]
	v_cndmask_b32_e64 v86, v86, v147, s[46:47]
	s_mov_b32 s45, 0x41d80000
	s_mov_b32 s43, 0x41c80000
	s_mov_b32 s41, 0x41980000
	s_mov_b32 s39, 0x41880000
	s_mov_b32 s37, 0x41300000
	s_mov_b32 s35, 0x40400000
	v_cndmask_b32_e64 v78, v78, v147, s[30:31]
	v_cndmask_b32_e64 v77, v77, v147, s[28:29]
	v_cndmask_b32_e64 v76, v76, v147, s[26:27]
	v_cndmask_b32_e64 v75, v75, v147, s[24:25]
	v_cndmask_b32_e64 v74, v74, v147, s[22:23]
	v_cndmask_b32_e64 v73, v73, v147, s[20:21]
	v_cndmask_b32_e64 v72, v72, v147, s[18:19]
	v_cndmask_b32_e64 v71, v71, v147, s[16:17]
	v_cndmask_b32_e64 v70, v70, v147, s[14:15]
	v_cndmask_b32_e64 v69, v69, v147, s[12:13]
	v_cndmask_b32_e64 v68, v68, v147, s[10:11]
	v_cndmask_b32_e64 v67, v67, v147, s[8:9]
	v_cndmask_b32_e32 v66, v66, v147, vcc
